# gla_scan: the 8 dv-slice workgroups of a (batch, head) mapped to one XCD (shared operands hit L2)
# speedup vs baseline: 1.0083x; 1.0083x over previous
.LBB0_825:
	s_cmpk_lt_i32 s96, 0x100
	v_mov_b32_e32 v2, v0
	s_cselect_b64 s[4:5], -1, 0
	s_cmpk_gt_i32 s96, 0xff
	s_movk_i32 s6, 0x100
	s_cbranch_scc1 .LBB0_839
	s_add_u32 s8, s84, 0x40600000
	s_addc_u32 s9, s85, 0
	s_add_u32 s10, s84, 0x11000000
	s_addc_u32 s11, s85, 0
	s_add_u32 s26, s84, 0x41000000
	v_readlane_b32 s18, v252, 6
	s_addc_u32 s27, s85, 0
	s_lshl_b32 s7, s18, 6
	s_add_u32 s14, s84, s7
	v_mov_b32_e32 v69, 0
	s_addc_u32 s15, s85, 0
	v_and_b32_e32 v66, 48, v2
	v_mov_b32_e32 v67, v69
	v_lshl_add_u64 v[4:5], s[14:15], 0, v[66:67]
	s_mov_b64 s[14:15], 0x40e00000
	s_lshl_b32 s16, s18, 3
	v_and_b32_e32 v7, 15, v2
	v_lshl_add_u64 v[70:71], v[4:5], 0, s[14:15]
	v_ashrrev_i32_e32 v3, 31, v2
	v_lshrrev_b32_e32 v11, 2, v2
	v_lshlrev_b32_e32 v13, 4, v2
	s_movk_i32 s14, 0x48
	v_readlane_b32 s17, v252, 0
	s_and_b32 s16, s16, 0x1ffffff0
	v_bfe_u32 v8, v2, 4, 2
	v_lshlrev_b64 v[4:5], 3, v[2:3]
	v_and_b32_e32 v13, 0xf0, v13
	v_ashrrev_i32_e32 v92, 3, v2
	s_movk_i32 s12, 0x90
	v_mul_lo_u32 v11, v11, s14
	v_lshl_add_u64 v[72:73], v[2:3], 4, s[8:9]
	s_bfe_u32 s15, s17, 0x10006
	v_or_b32_e32 v3, s16, v7
	v_lshlrev_b32_e32 v10, 2, v8
	v_add_u32_e32 v14, 0, v13
	v_mul_lo_u32 v13, v92, s12
	v_add_u32_e32 v17, 0, v11
	v_mul_lo_u32 v11, v3, s12
	v_lshlrev_b32_e32 v19, 3, v8
	s_lshl_b32 s12, s15, 5
	v_lshlrev_b32_e32 v8, 3, v2
	v_add_u32_e32 v15, 0, v13
	v_and_b32_e32 v13, 7, v2
	v_and_b32_e32 v8, 24, v8
	s_add_i32 s12, s12, 0
	v_add_u32_e32 v93, 0, v11
	v_add_u32_e32 v94, s12, v8
	v_add_u32_e32 v96, 0, v8
	v_or_b32_e32 v21, s16, v10
	v_mul_lo_u32 v11, v92, 36
	v_lshlrev_b32_e32 v8, 2, v13
	v_lshl_or_b32 v24, s18, 4, v10
	v_add_u32_e32 v10, 0x200, v2
	v_bfe_u32 v9, v2, 2, 2
	v_and_b32_e32 v12, 3, v2
	v_add_lshl_u32 v23, v11, v8, 2
	v_ashrrev_i32_e32 v11, 31, v10
	v_lshlrev_b32_e32 v6, 3, v12
	v_lshlrev_b32_e32 v16, 4, v13
	v_lshlrev_b32_e32 v18, 4, v12
	v_lshl_add_u32 v95, v3, 7, v93
	v_or_b32_e32 v3, v19, v9
	v_lshlrev_b64 v[12:13], 3, v[10:11]
	v_lshrrev_b32_e32 v11, 4, v2
	s_movk_i32 s12, 0x110
	v_lshrrev_b32_e32 v10, 4, v10
	v_or_b32_e32 v25, 32, v19
	v_or_b32_e32 v26, 64, v19
	v_or_b32_e32 v19, 0x60, v19
	v_mul_lo_u32 v11, v11, s12
	v_mul_lo_u32 v10, v10, s12
	v_mul_u32_u24_e32 v97, 0x48, v3
	v_lshlrev_b32_e32 v98, 1, v25
	v_or_b32_e32 v25, v25, v9
	v_lshlrev_b32_e32 v27, 1, v26
	v_or_b32_e32 v26, v26, v9
	v_lshlrev_b32_e32 v28, 1, v19
	v_or_b32_e32 v9, v19, v9
	v_mul_u32_u24_e32 v19, 0x110, v3
	v_or_b32_e32 v3, 32, v3
	s_and_b32 s12, s17, 0xffffffc0
	v_lshl_or_b32 v22, s15, 4, v7
	v_mul_u32_u24_e32 v29, 0x48, v3
	v_mul_lo_u32 v3, v21, 36
	v_mul_lo_u32 v24, v24, s14
	s_add_u32 s14, s84, s12
	s_movk_i32 s0, 0x900
	v_add_lshl_u32 v99, v3, v22, 2
	v_lshl_add_u32 v3, v2, 2, 0
	s_addc_u32 s15, s85, 0
	v_cmp_gt_i32_e64 s[0:1], s0, v2
	v_bfe_u32 v1, v2, 2, 6
	v_cmp_gt_i32_e64 s[6:7], s6, v2
	v_lshl_add_u32 v20, s18, 5, v96
	v_lshl_add_u32 v7, v7, 1, 0
	v_mul_u32_u24_e32 v25, 0x48, v25
	v_mul_u32_u24_e32 v26, 0x48, v26
	v_mul_u32_u24_e32 v9, 0x48, v9
	v_add_u32_e32 v21, 0x90, v99
	v_add_u32_e32 v22, 0x120, v99
	v_add_u32_e32 v30, 0x1b0, v99
	v_add_u32_e32 v100, 0xbe00, v3
	v_add_u32_e32 v101, 0xfffffe00, v2
	v_lshl_add_u64 v[2:3], s[14:15], 0, v[66:67]
	s_mov_b64 s[14:15], 0x40e00200
	s_mov_b32 s12, 0xac00
	s_mov_b32 s13, 0
	v_lshl_add_u64 v[74:75], v[2:3], 0, s[14:15]
	s_movk_i32 s28, 0x6ff
	v_lshlrev_b32_e32 v68, 1, v6
	s_movk_i32 s29, 0x2000
	v_lshlrev_b32_e32 v76, 2, v8
	s_mov_b64 s[14:15], 0x400
	v_lshlrev_b64 v[78:79], 1, v[4:5]
	v_lshlrev_b64 v[80:81], 1, v[12:13]
	v_add_u32_e32 v67, v14, v11
	v_add_u32_e32 v102, v14, v10
	v_add_u32_e32 v103, v15, v16
	v_add3_u32 v104, v17, v18, s12
	v_add_u32_e32 v105, v94, v25
	v_add_u32_e32 v106, v95, v27
	v_add_u32_e32 v107, v94, v26
	v_add_u32_e32 v108, v95, v28
	v_add_u32_e32 v109, v94, v9
	v_add_u32_e32 v110, v20, v19
	v_add_u32_e32 v111, v96, v29
	v_add_u32_e32 v112, 0, v21
	v_add_u32_e32 v113, 0, v22
	v_add_u32_e32 v114, 0, v30
	v_add_u32_e32 v115, 0, v23
	v_add_u32_e32 v116, v7, v24
	s_mov_b32 s30, s96
	s_cmpk_lg_i32 s43, 0x100
	s_cbranch_scc1 .Lmy_gs_nomap
	s_and_b32 s30, s96, 7
	s_lshl_b32 s30, s30, 2
	s_lshr_b32 s100, s96, 6
	s_add_i32 s30, s30, s100
	s_lshl_b32 s30, s30, 3
	s_bfe_u32 s100, s96, 0x30003
	s_add_i32 s30, s30, s100
.Lmy_gs_nomap:
	s_branch .LBB0_828
.LBB0_827:
	s_waitcnt lgkmcnt(0)
	s_barrier
	s_add_i32 s30, s30, s43
	s_cmpk_gt_i32 s30, 0xff
	s_cbranch_scc1 .LBB0_839
